# attention phase: one static s_setprio 1 for waves 4-7 (docs 6.3)
# baseline (speedup 1.0000x reference)
; #define LAS __attribute__((address_space(3)))
;     DI unsigned char* wsp() const { return (unsigned char*)ws_g; }
;     DI const float* inp(int i) const { return (const float*)(*(const GAS float* const __attribute__((address_space(4)))*)(ka + 8 * i)); }
; #define FRESH() do { asm volatile("" : "+s"(F.wave)); int l_ = (int)__builtin_amdgcn_mbcnt_hi(~0u, __builtin_amdgcn_mbcnt_lo(~0u, 0u)); asm volatile("" : "+v"(l_)); F.lane = l_; F.tid = F.wave * 64 + l_; } while (0)
; #define PHASE(k) if (IN(P + (k))) for (int rep_ = 0; rep_ < NREP(k); ++rep_)
;     static constexpr unsigned PIECES[NPIECE] = {1179905,1638914,786432,2032387,2032644,2032901,2033158,2033415,2033672,2033929,2034186,2034443,2034700,2034957,2035214,2035471,2035728,2034944,2035985,2036242,2036499,2036756,2037013,2037270,2037527,2037784,2038041,2036481,2038298,2038555,2038812,2039069,2039326,2039583,2038274};
;     LAS unsigned char* Ks = F.lds;
;     LAS unsigned char* Vt = F.lds + 36864;
;     LAS float* LUT = (LAS float*)(F.lds + 36864 + 33280);
;     LAS unsigned* CTL = (LAS unsigned*)(F.lds + 36864 + 33280 + 528);
;     LAS unsigned* LIST = CTL + 4;
;     const bf16_t* MO = (const bf16_t*)(F.wsp() + WS_MO); const unsigned* SEL = (const unsigned*)(F.wsp() + WS_SEL);
;     bf16_t* PO = (bf16_t*)(F.wsp() + WS_PO); f32x2* PST = (f32x2*)(F.wsp() + WS_PST);
;     unsigned* qctr = (unsigned*)(F.wsp() + WS_CTL) + CW_QATT + 64 * l + 32 * rep;
;     const float* relb = F.inp(25);
;     const int lane = F.lane;
;     bool att_done = false, conv_done = false;
;     unsigned nu = 0u; if (F.tid == 0) nu = __hip_atomic_fetch_add(qctr, 1u, __ATOMIC_RELAXED, __HIP_MEMORY_SCOPE_AGENT);
; __global__ void __launch_bounds__(512, 2) fwd_kernel(Args args) {
;     ...
;         PHASE(9) { FRESH(); phase_moba_attn(F, l, rep_); }
.LBB0_1782:
	s_cmp_le_i32 s96, s22
	s_cselect_b64 s[2:3], -1, 0
	s_and_b64 s[36:37], s[2:3], s[0:1]
	v_readlane_b32 s0, v252, 17
	v_readlane_b32 s1, v252, 18
	v_readlane_b32 s2, v252, 19
	v_readlane_b32 s3, v252, 20
	s_andn2_b64 vcc, exec, s[36:37]
	v_writelane_b32 v252, s2, 19
	s_nop 1
	v_writelane_b32 v252, s3, 20
	v_writelane_b32 v252, s0, 17
	s_nop 1
	v_writelane_b32 v252, s1, 18
	s_cbranch_vccnz .LBB0_2249
	s_lshl_b32 s44, s50, 6
	s_lshl_b64 s[0:1], s[44:45], 2
	s_add_u32 s0, s94, s0
	s_addc_u32 s1, s95, s1
	v_mov_b32_e32 v0, v230
	s_add_u32 s38, s0, 0x8000
	s_addc_u32 s39, s1, 0
	v_lshl_add_u32 v147, s68, 6, v0
	s_cmp_ge_u32 s68, 4
	s_cbranch_scc0 .Lattn_prio_done
	s_setprio 1
.Lattn_prio_done:
	v_mov_b32_e32 v153, 0
	v_cmp_eq_u32_e64 s[8:9], 0, v147
	s_and_saveexec_b64 s[0:1], s[8:9]
	s_cbranch_execz .LBB0_1787
	s_mov_b64 s[4:5], exec
	v_mbcnt_lo_u32_b32 v1, s4, 0
	v_mbcnt_hi_u32_b32 v1, s5, v1
	v_cmp_eq_u32_e32 vcc, 0, v1
	s_and_saveexec_b64 s[2:3], vcc
	s_cbranch_execz .LBB0_1786
	s_bcnt1_i32_b64 s4, s[4:5]
	v_mov_b32_e32 v2, s4
	global_atomic_add v2, v65, v2, s[38:39] sc0

; #define SEAM(k) do { asm volatile("" : "+s"(barp), "+s"(bar.x)); bar.bar = (unsigned*)barp; if (IN(k) && IN((k) + 1)) xcd_barrier(bar); asm volatile("" : "+s"(F.ws_g), "+s"(F.out_g), "+s"(F.ka), "+s"(F.bid), "+s"(F.G), "+s"(F.lds)); } while (0)
; __device__ __forceinline__ void xcd_barrier(const XcdBarrier& b) {
;     asm volatile("s_waitcnt vmcnt(0)" ::: "memory");
;     __syncthreads();
;     if (threadIdx.x == 0) {
;         unsigned* bar = b.bar;
;         __builtin_amdgcn_s_waitcnt(0);
;         unsigned nloc = b.st[0], nx = b.st[1];
;         if (nloc == 0u) { xcd_barrier_complete(bar, b.x, nloc, nx); b.st[0] = nloc; b.st[1] = nx; }
; __global__ void __launch_bounds__(512, 2) fwd_kernel(Args args) {
;     ...
;         SEAM(P + 9);
.LBB0_2249:
	s_setprio 0
	s_mul_i32 s0, s50, 19
	s_add_i32 s22, s0, 10
	s_cmp_lt_i32 s22, s97
	s_cselect_b64 s[0:1], -1, 0
	s_and_b64 s[2:3], s[36:37], s[0:1]
	s_andn2_b64 vcc, exec, s[2:3]
	v_readlane_b32 s2, v252, 3
	s_nop 1
	v_writelane_b32 v252, s2, 3
	s_cbranch_vccnz .LBB0_2303
	s_waitcnt vmcnt(0)
	s_waitcnt vmcnt(0) lgkmcnt(0)
	s_barrier
	s_mov_b64 s[2:3], exec
	v_readlane_b32 s4, v252, 15
	v_readlane_b32 s5, v252, 16
	s_and_b64 s[4:5], s[2:3], s[4:5]
	s_mov_b64 exec, s[4:5]
	s_cbranch_execz .LBB0_2302
	v_readlane_b32 s4, v252, 4
	s_waitcnt vmcnt(0) expcnt(0) lgkmcnt(0)
	s_nop 0
	v_mov_b32_e32 v0, s4
	ds_read_b32 v2, v0
	ds_read_b32 v0, v0 offset:4
	s_waitcnt lgkmcnt(1)
	v_cmp_ne_u32_e32 vcc, 0, v2
	s_cbranch_vccnz .LBB0_2266
	v_readlane_b32 s4, v252, 1
	v_readlane_b32 s5, v252, 2
	s_load_dwordx2 s[8:9], s[4:5], 0x4
	s_add_u32 s4, s92, 0x1000
	s_addc_u32 s5, s93, 0
	s_add_u32 s6, s92, 0x1100
	s_addc_u32 s7, s93, 0
	v_readlane_b32 s10, v252, 0
	s_waitcnt lgkmcnt(0)
	s_mul_i32 s18, s8, s10
	s_add_u32 s8, s92, 0x1200
	s_mul_i32 s18, s18, s9
	s_addc_u32 s9, s93, 0
	s_add_u32 s10, s92, 0x1300
	s_addc_u32 s11, s93, 0
	s_mov_b32 s19, 1
	s_branch .LBB0_2254
